# expert-weight conversion loop restructured as a two-stage software pipeline (loads of next item issued per 16-row half, counted vmcnt waits)
# baseline (speedup 1.0000x reference)
.LBB0_243:
	s_cmp_lg_u32 s83, s81
	s_cbranch_scc1 .LBB0_255
	v_readlane_b32 s6, v254, 15
	v_readlane_b32 s7, v254, 16
	v_mov_b32_e32 v137, v1
	s_andn2_b64 vcc, exec, s[6:7]
	s_cbranch_vccnz .LBB0_254
	v_lshlrev_b32_e32 v132, 2, v137
	v_readlane_b32 s6, v254, 39
	v_ashrrev_i32_e32 v133, 31, v132
	v_readlane_b32 s7, v254, 40
	v_ashrrev_i32_e32 v0, 4, v137
	v_add_u32_e32 v135, s69, v0
	s_waitcnt vmcnt(39)
	v_lshl_add_u64 v[120:121], v[132:133], 2, s[6:7]
	v_readlane_b32 s6, v254, 41
	v_readlane_b32 s7, v254, 42
	v_and_b32_e32 v153, 15, v137
	v_lshrrev_b32_e32 v0, 2, v0
	v_lshl_add_u64 v[122:123], v[120:121], 0, s[6:7]
	v_readlane_b32 s6, v254, 43
	v_readlane_b32 s7, v254, 44
	v_bitop3_b32 v0, v0, v153, 7 bitop3:0x6c
	v_lshlrev_b32_e32 v139, 4, v0
	s_waitcnt vmcnt(10)
	v_lshl_add_u64 v[4:5], v[120:121], 0, s[6:7]
	v_readlane_b32 s6, v254, 45
	v_readlane_b32 s7, v254, 46
	v_add_u32_e32 v0, 4, v135
	v_lshlrev_b32_e32 v140, 8, v0
	v_lshl_add_u64 v[6:7], v[120:121], 0, s[6:7]
	v_readlane_b32 s6, v254, 47
	v_readlane_b32 s7, v254, 48
	global_load_dwordx4 v[8:11], v[4:5], off nt
	s_nop 0
	global_load_dwordx4 v[4:7], v[6:7], off nt
	v_lshl_add_u64 v[12:13], v[120:121], 0, s[6:7]
	v_readlane_b32 s6, v254, 49
	v_readlane_b32 s7, v254, 50
	v_lshrrev_b32_e32 v0, 2, v0
	v_bitop3_b32 v0, v0, v153, 7 bitop3:0x6c
	v_lshl_add_u64 v[14:15], v[120:121], 0, s[6:7]
	v_readlane_b32 s6, v254, 51
	v_readlane_b32 s7, v254, 52
	global_load_dwordx4 v[16:19], v[12:13], off nt
	s_nop 0
	global_load_dwordx4 v[12:15], v[14:15], off nt
	v_lshl_add_u64 v[20:21], v[120:121], 0, s[6:7]
	v_readlane_b32 s6, v254, 53
	v_readlane_b32 s7, v254, 54
	v_lshlrev_b32_e32 v141, 4, v0
	v_add_u32_e32 v0, 8, v135
	v_lshl_add_u64 v[22:23], v[120:121], 0, s[6:7]
	v_readlane_b32 s6, v254, 55
	v_readlane_b32 s7, v254, 56
	global_load_dwordx4 v[24:27], v[20:21], off nt
	s_nop 0
	global_load_dwordx4 v[20:23], v[22:23], off nt
	v_lshl_add_u64 v[28:29], v[120:121], 0, s[6:7]
	v_readlane_b32 s6, v254, 57
	v_readlane_b32 s7, v254, 58
	v_lshlrev_b32_e32 v142, 8, v0
	v_lshrrev_b32_e32 v0, 2, v0
	v_lshl_add_u64 v[30:31], v[120:121], 0, s[6:7]
	v_readlane_b32 s6, v254, 59
	v_readlane_b32 s7, v254, 60
	global_load_dwordx4 v[32:35], v[28:29], off nt
	s_nop 0
	global_load_dwordx4 v[28:31], v[30:31], off nt
	v_lshl_add_u64 v[36:37], v[120:121], 0, s[6:7]
	v_readlane_b32 s6, v254, 61
	v_readlane_b32 s7, v254, 62
	v_bitop3_b32 v0, v0, v153, 7 bitop3:0x6c
	v_lshlrev_b32_e32 v143, 4, v0
	v_lshl_add_u64 v[38:39], v[120:121], 0, s[6:7]
	v_readlane_b32 s6, v254, 63
	v_readlane_b32 s7, v255, 0
	global_load_dwordx4 v[40:43], v[36:37], off nt
	s_nop 0
	global_load_dwordx4 v[36:39], v[38:39], off nt
	v_lshl_add_u64 v[44:45], v[120:121], 0, s[6:7]
	v_readlane_b32 s6, v255, 1
	v_readlane_b32 s7, v255, 2
	v_add_u32_e32 v0, 12, v135
	v_lshlrev_b32_e32 v144, 8, v0
	v_lshl_add_u64 v[46:47], v[120:121], 0, s[6:7]
	v_readlane_b32 s6, v255, 3
	v_readlane_b32 s7, v255, 4
	global_load_dwordx4 v[48:51], v[44:45], off nt
	s_nop 0
	global_load_dwordx4 v[44:47], v[46:47], off nt
	v_lshl_add_u64 v[52:53], v[120:121], 0, s[6:7]
	v_readlane_b32 s6, v255, 5
	v_readlane_b32 s7, v255, 6
	v_lshrrev_b32_e32 v0, 2, v0
	v_bitop3_b32 v0, v0, v153, 7 bitop3:0x6c
	v_lshl_add_u64 v[54:55], v[120:121], 0, s[6:7]
	v_readlane_b32 s6, v255, 7
	v_readlane_b32 s7, v255, 8
	global_load_dwordx4 v[56:59], v[52:53], off nt
	s_nop 0
	global_load_dwordx4 v[52:55], v[54:55], off nt
	v_lshl_add_u64 v[92:93], v[120:121], 0, s[6:7]
	v_readlane_b32 s6, v255, 11
	v_readlane_b32 s7, v255, 12
	v_lshlrev_b32_e32 v145, 4, v0
	v_add_u32_e32 v0, 16, v135
	v_lshl_add_u64 v[60:61], v[120:121], 0, s[6:7]
	v_readlane_b32 s6, v255, 13
	v_readlane_b32 s7, v255, 14
	global_load_dwordx4 v[64:67], v[92:93], off nt
	s_nop 0
	global_load_dwordx4 v[60:63], v[60:61], off nt
	v_lshl_add_u64 v[68:69], v[120:121], 0, s[6:7]
	v_readlane_b32 s6, v255, 15
	v_readlane_b32 s7, v255, 16
	v_lshlrev_b32_e32 v146, 8, v0
	v_lshrrev_b32_e32 v0, 2, v0
	v_lshl_add_u64 v[70:71], v[120:121], 0, s[6:7]
	v_readlane_b32 s6, v255, 17
	v_readlane_b32 s7, v255, 18
	global_load_dwordx4 v[72:75], v[68:69], off nt
	s_nop 0
	global_load_dwordx4 v[68:71], v[70:71], off nt
	v_lshl_add_u64 v[76:77], v[120:121], 0, s[6:7]
	v_readlane_b32 s6, v255, 19
	v_readlane_b32 s7, v255, 20
	v_bitop3_b32 v0, v0, v153, 7 bitop3:0x6c
	v_lshlrev_b32_e32 v147, 4, v0
	v_lshl_add_u64 v[78:79], v[120:121], 0, s[6:7]
	v_readlane_b32 s6, v255, 21
	v_readlane_b32 s7, v255, 22
	global_load_dwordx4 v[80:83], v[76:77], off nt
	s_nop 0
	global_load_dwordx4 v[76:79], v[78:79], off nt
	v_lshl_add_u64 v[84:85], v[120:121], 0, s[6:7]
	v_readlane_b32 s6, v255, 23
	v_readlane_b32 s7, v255, 24
	v_add_u32_e32 v0, 20, v135
	v_lshlrev_b32_e32 v148, 8, v0
	v_lshl_add_u64 v[86:87], v[120:121], 0, s[6:7]
	v_readlane_b32 s6, v255, 33
	v_readlane_b32 s7, v255, 34
	global_load_dwordx4 v[88:91], v[84:85], off nt
	s_nop 0
	global_load_dwordx4 v[84:87], v[86:87], off nt
	v_lshl_add_u64 v[108:109], v[92:93], 0, s[6:7]
	v_readlane_b32 s6, v255, 25
	v_readlane_b32 s7, v255, 26
	v_lshrrev_b32_e32 v0, 2, v0
	v_bitop3_b32 v0, v0, v153, 7 bitop3:0x6c
	v_lshl_add_u64 v[92:93], v[120:121], 0, s[6:7]
	v_readlane_b32 s6, v255, 27
	v_readlane_b32 s7, v255, 28
	global_load_dwordx4 v[96:99], v[108:109], off nt
	s_nop 0
	global_load_dwordx4 v[92:95], v[92:93], off nt
	v_lshl_add_u64 v[100:101], v[120:121], 0, s[6:7]
	v_readlane_b32 s6, v255, 29
	v_readlane_b32 s7, v255, 30
	v_lshlrev_b32_e32 v149, 4, v0
	v_add_u32_e32 v0, 24, v135
	v_lshl_add_u64 v[102:103], v[120:121], 0, s[6:7]
	v_readlane_b32 s6, v255, 35
	v_readlane_b32 s7, v255, 36
	global_load_dwordx4 v[104:107], v[100:101], off nt
	s_nop 0
	global_load_dwordx4 v[100:103], v[102:103], off nt
	v_lshl_add_u64 v[116:117], v[108:109], 0, s[6:7]
	v_readlane_b32 s6, v255, 31
	v_readlane_b32 s7, v255, 32
	v_lshlrev_b32_e32 v150, 8, v0
	v_lshrrev_b32_e32 v0, 2, v0
	v_lshl_add_u64 v[108:109], v[120:121], 0, s[6:7]
	v_readlane_b32 s6, v255, 37
	v_readlane_b32 s7, v255, 38
	global_load_dwordx4 v[112:115], v[116:117], off nt
	s_nop 0
	global_load_dwordx4 v[108:111], v[108:109], off nt
	v_lshl_add_u64 v[116:117], v[116:117], 0, s[6:7]
	v_readlane_b32 s6, v255, 39
	v_readlane_b32 s7, v255, 40
	v_bitop3_b32 v0, v0, v153, 7 bitop3:0x6c
	v_lshlrev_b32_e32 v134, 10, v137
	v_lshl_add_u64 v[118:119], v[116:117], 0, s[6:7]
	global_load_dwordx4 v[124:127], v[116:117], off nt
	s_nop 0
	global_load_dwordx4 v[116:119], v[118:119], off nt
	s_nop 0
	global_load_dwordx4 v[128:131], v[122:123], off nt
	s_nop 0
	global_load_dwordx4 v[120:123], v[120:121], off nt
	v_readlane_b32 s6, v254, 17
	v_lshlrev_b32_e32 v2, 4, v137
	v_lshlrev_b32_e32 v151, 4, v0
	v_bitop3_b32 v136, v137, s6, 7 bitop3:0x6c
	v_readlane_b32 s6, v254, 21
	v_add_u32_e32 v0, 28, v135
	v_lshlrev_b32_e32 v152, 8, v0
	v_bitop3_b32 v137, v137, s6, 7 bitop3:0x6c
	s_add_i32 s6, s33, s94
	v_lshrrev_b32_e32 v0, 2, v0
	s_lshl_b32 s10, s6, 5
	s_lshl_b32 s44, s6, 8
	v_readlane_b32 s6, v254, 30
	v_readlane_b32 s14, v254, 37
	v_bitop3_b32 v0, v0, v153, 7 bitop3:0x6c
	v_readlane_b32 s7, v254, 31
	v_readlane_b32 s67, v254, 36
	v_readlane_b32 s15, v254, 38
	v_and_b32_e32 v2, 0xf0, v2
	v_lshlrev_b32_e32 v136, 4, v136
	v_lshlrev_b32_e32 v137, 4, v137
	v_lshlrev_b32_e32 v138, 8, v135
	v_lshlrev_b32_e32 v153, 4, v0
	s_lshl_b32 s11, s33, 5
	s_lshl_b32 s53, s33, 8
	s_mov_b32 s62, 0
	s_mov_b32 s63, s94
	s_mov_b32 s66, s14
	v_mov_b32_e32 v155, v215
	s_mov_b64 s[14:15], s[6:7]
	s_mov_b32 s64, s67
	v_mov_b32_e32 v154, v215
	s_waitcnt vmcnt(0)
	s_branch .LBB0_249

.LBB0_249:
	s_lshl_b32 s42, s62, 16
	s_add_i32 s65, s42, 0
	v_add_u32_e32 v0, s65, v134
	v_add_u32_e32 v157, v0, v136
	v_add_u32_e32 v156, v0, v137
	s_waitcnt vmcnt(24)
	v_mul_f32_e32 v162, 0x42000000, v120
	v_mul_f32_e32 v163, 0x42000000, v116
	v_mul_f32_e32 v164, 0x42000000, v124
	v_cvt_pk_fp8_f32 v158, v162, v163
	v_mul_f32_e32 v165, 0x42000000, v108
	v_cvt_pk_fp8_f32 v158, v164, v165 op_sel:[0,0,1]
	v_mul_f32_e32 v162, 0x42000000, v112
	v_mul_f32_e32 v163, 0x42000000, v100
	v_mul_f32_e32 v164, 0x42000000, v104
	v_cvt_pk_fp8_f32 v159, v162, v163
	v_mul_f32_e32 v165, 0x42000000, v92
	v_cvt_pk_fp8_f32 v159, v164, v165 op_sel:[0,0,1]
	v_mul_f32_e32 v162, 0x42000000, v96
	v_mul_f32_e32 v163, 0x42000000, v84
	v_mul_f32_e32 v164, 0x42000000, v88
	v_cvt_pk_fp8_f32 v160, v162, v163
	v_mul_f32_e32 v165, 0x42000000, v76
	v_cvt_pk_fp8_f32 v160, v164, v165 op_sel:[0,0,1]
	v_mul_f32_e32 v162, 0x42000000, v80
	v_mul_f32_e32 v163, 0x42000000, v68
	v_mul_f32_e32 v164, 0x42000000, v72
	v_cvt_pk_fp8_f32 v161, v162, v163
	v_mul_f32_e32 v165, 0x42000000, v60
	v_cvt_pk_fp8_f32 v161, v164, v165 op_sel:[0,0,1]
	ds_write_b128 v157, v[158:161]
	v_mul_f32_e32 v162, 0x42000000, v121
	v_mul_f32_e32 v163, 0x42000000, v117
	v_mul_f32_e32 v164, 0x42000000, v125
	v_cvt_pk_fp8_f32 v168, v162, v163
	v_mul_f32_e32 v165, 0x42000000, v109
	v_cvt_pk_fp8_f32 v168, v164, v165 op_sel:[0,0,1]
	v_mul_f32_e32 v162, 0x42000000, v113
	v_mul_f32_e32 v163, 0x42000000, v101
	v_mul_f32_e32 v164, 0x42000000, v105
	v_cvt_pk_fp8_f32 v169, v162, v163
	v_mul_f32_e32 v165, 0x42000000, v93
	v_cvt_pk_fp8_f32 v169, v164, v165 op_sel:[0,0,1]
	v_mul_f32_e32 v162, 0x42000000, v97
	v_mul_f32_e32 v163, 0x42000000, v85
	v_mul_f32_e32 v164, 0x42000000, v89
	v_cvt_pk_fp8_f32 v170, v162, v163
	v_mul_f32_e32 v165, 0x42000000, v77
	v_cvt_pk_fp8_f32 v170, v164, v165 op_sel:[0,0,1]
	v_mul_f32_e32 v162, 0x42000000, v81
	v_mul_f32_e32 v163, 0x42000000, v69
	v_mul_f32_e32 v164, 0x42000000, v73
	v_cvt_pk_fp8_f32 v171, v162, v163
	v_mul_f32_e32 v165, 0x42000000, v61
	v_cvt_pk_fp8_f32 v171, v164, v165 op_sel:[0,0,1]
	ds_write_b128 v157, v[168:171] offset:256
	v_mul_f32_e32 v162, 0x42000000, v122
	v_mul_f32_e32 v163, 0x42000000, v118
	v_mul_f32_e32 v164, 0x42000000, v126
	v_cvt_pk_fp8_f32 v158, v162, v163
	v_mul_f32_e32 v165, 0x42000000, v110
	v_cvt_pk_fp8_f32 v158, v164, v165 op_sel:[0,0,1]
	v_mul_f32_e32 v162, 0x42000000, v114
	v_mul_f32_e32 v163, 0x42000000, v102
	v_mul_f32_e32 v164, 0x42000000, v106
	v_cvt_pk_fp8_f32 v159, v162, v163
	v_mul_f32_e32 v165, 0x42000000, v94
	v_cvt_pk_fp8_f32 v159, v164, v165 op_sel:[0,0,1]
	v_mul_f32_e32 v162, 0x42000000, v98
	v_mul_f32_e32 v163, 0x42000000, v86
	v_mul_f32_e32 v164, 0x42000000, v90
	v_cvt_pk_fp8_f32 v160, v162, v163
	v_mul_f32_e32 v165, 0x42000000, v78
	v_cvt_pk_fp8_f32 v160, v164, v165 op_sel:[0,0,1]
	v_mul_f32_e32 v162, 0x42000000, v82
	v_mul_f32_e32 v163, 0x42000000, v70
	v_mul_f32_e32 v164, 0x42000000, v74
	v_cvt_pk_fp8_f32 v161, v162, v163
	v_mul_f32_e32 v165, 0x42000000, v62
	v_cvt_pk_fp8_f32 v161, v164, v165 op_sel:[0,0,1]
	ds_write_b128 v157, v[158:161] offset:512
	v_mul_f32_e32 v162, 0x42000000, v123
	v_mul_f32_e32 v163, 0x42000000, v119
	v_mul_f32_e32 v164, 0x42000000, v127
	v_cvt_pk_fp8_f32 v168, v162, v163
	v_mul_f32_e32 v165, 0x42000000, v111
	v_cvt_pk_fp8_f32 v168, v164, v165 op_sel:[0,0,1]
	v_mul_f32_e32 v162, 0x42000000, v115
	v_mul_f32_e32 v163, 0x42000000, v103
	v_mul_f32_e32 v164, 0x42000000, v107
	v_cvt_pk_fp8_f32 v169, v162, v163
	v_mul_f32_e32 v165, 0x42000000, v95
	v_cvt_pk_fp8_f32 v169, v164, v165 op_sel:[0,0,1]
	v_mul_f32_e32 v162, 0x42000000, v99
	v_mul_f32_e32 v163, 0x42000000, v87
	v_mul_f32_e32 v164, 0x42000000, v91
	v_cvt_pk_fp8_f32 v170, v162, v163
	v_mul_f32_e32 v165, 0x42000000, v79
	v_cvt_pk_fp8_f32 v170, v164, v165 op_sel:[0,0,1]
	v_mul_f32_e32 v162, 0x42000000, v83
	v_mul_f32_e32 v163, 0x42000000, v71
	v_mul_f32_e32 v164, 0x42000000, v75
	v_cvt_pk_fp8_f32 v171, v162, v163
	v_mul_f32_e32 v165, 0x42000000, v63
	v_cvt_pk_fp8_f32 v171, v164, v165 op_sel:[0,0,1]
	ds_write_b128 v157, v[168:171] offset:768
	s_add_i32 s63, s63, s33
	s_cmpk_gt_i32 s63, 0x17ff
	s_cselect_b64 s[54:55], -1, 0
	s_and_b64 vcc, exec, s[54:55]
	s_mov_b32 s56, s66
	s_cbranch_vccnz .Lcv_nonext
	s_cmpk_gt_i32 s63, 0xfff
	s_mov_b64 s[60:61], -1
	s_cbranch_scc0 .LBB0_252
	s_add_i32 s14, s63, 0xfffff000
	s_lshr_b32 s42, s14, 6
	s_lshl_b64 s[14:15], s[42:43], 22
	s_lshl_b64 s[56:57], s[42:43], 24
	s_add_u32 s58, s24, s56
	s_addc_u32 s59, s25, s57
	s_add_u32 s14, s16, s14
	s_addc_u32 s15, s17, s15
	s_and_b32 s64, s10, 0x700
	s_and_b32 s56, s44, 0x700
	s_mov_b64 s[60:61], 0
.LBB0_252:
	s_andn2_b64 vcc, exec, s[60:61]
	s_cbranch_vccz .LBB0_246
	s_mov_b64 s[60:61], 0x800
	s_mov_b32 s61, 0
	s_branch .LBB0_247
.LBB0_246:
	s_ashr_i32 s14, s63, 31
	s_lshr_b32 s14, s14, 25
	s_add_i32 s15, s63, s14
	s_ashr_i32 s14, s15, 7
	s_and_b32 s15, s15, 0xff80
	s_sub_i32 s42, s63, s15
	s_ashr_i32 s15, s14, 31
	s_lshl_b64 s[56:57], s[14:15], 25
	s_add_u32 s58, s20, s56
	s_addc_u32 s59, s21, s57
	s_lshl_b64 s[14:15], s[14:15], 23
	s_add_u32 s14, s40, s14
	s_addc_u32 s15, s41, s15
	s_bfe_i32 s56, s42, 0x80000
	s_bfe_u32 s56, s56, 0x4000b
	s_add_i32 s56, s42, s56
	s_bfe_i32 s57, s56, 0x80000
	s_and_b32 s56, s56, 0xf0
	s_sext_i32_i16 s57, s57
	s_sub_i32 s42, s42, s56
	s_lshl_b32 s57, s57, 4
	s_sext_i32_i8 s42, s42
	s_mov_b64 s[60:61], 0x1000
	s_and_b32 s64, s57, 0xffffff00
	s_lshl_b32 s56, s42, 8
	s_mov_b32 s61, 1
.LBB0_247:
	s_add_i32 s42, s64, s69
	s_mul_hi_i32 s71, s60, s42
	s_mul_i32 s70, s60, s42
	s_lshl_b64 s[70:71], s[70:71], 2
	s_add_u32 s42, s58, s70
	s_addc_u32 s70, s59, s71
	s_ashr_i32 s57, s56, 31
	s_lshl_b64 s[58:59], s[56:57], 2
	s_add_u32 s58, s42, s58
	s_addc_u32 s59, s70, s59
	s_lshl_b32 s42, s60, 2
	v_lshl_add_u64 v[166:167], v[132:133], 2, s[58:59]
	global_load_dwordx4 v[120:123], v[166:167], off nt
	v_lshl_add_u64 v[172:173], v[166:167], 0, s[42:43]
	global_load_dwordx4 v[116:119], v[172:173], off nt
	v_lshl_add_u64 v[166:167], v[172:173], 0, s[42:43]
	global_load_dwordx4 v[124:127], v[166:167], off nt
	v_lshl_add_u64 v[172:173], v[166:167], 0, s[42:43]
	global_load_dwordx4 v[108:111], v[172:173], off nt
	v_lshl_add_u64 v[166:167], v[172:173], 0, s[42:43]
	global_load_dwordx4 v[112:115], v[166:167], off nt
	v_lshl_add_u64 v[172:173], v[166:167], 0, s[42:43]
	global_load_dwordx4 v[100:103], v[172:173], off nt
	v_lshl_add_u64 v[166:167], v[172:173], 0, s[42:43]
	global_load_dwordx4 v[104:107], v[166:167], off nt
	v_lshl_add_u64 v[172:173], v[166:167], 0, s[42:43]
	global_load_dwordx4 v[92:95], v[172:173], off nt
	v_lshl_add_u64 v[166:167], v[172:173], 0, s[42:43]
	global_load_dwordx4 v[96:99], v[166:167], off nt
	v_lshl_add_u64 v[172:173], v[166:167], 0, s[42:43]
	global_load_dwordx4 v[84:87], v[172:173], off nt
	v_lshl_add_u64 v[166:167], v[172:173], 0, s[42:43]
	global_load_dwordx4 v[88:91], v[166:167], off nt
	v_lshl_add_u64 v[172:173], v[166:167], 0, s[42:43]
	global_load_dwordx4 v[76:79], v[172:173], off nt
	v_lshl_add_u64 v[166:167], v[172:173], 0, s[42:43]
	global_load_dwordx4 v[80:83], v[166:167], off nt
	v_lshl_add_u64 v[172:173], v[166:167], 0, s[42:43]
	global_load_dwordx4 v[68:71], v[172:173], off nt
	v_lshl_add_u64 v[166:167], v[172:173], 0, s[42:43]
	global_load_dwordx4 v[72:75], v[166:167], off nt
	v_lshl_add_u64 v[172:173], v[166:167], 0, s[42:43]
	global_load_dwordx4 v[60:63], v[172:173], off nt
	v_lshl_add_u64 v[166:167], v[172:173], 0, s[42:43]
	s_waitcnt vmcnt(24)
	v_mul_f32_e32 v162, 0x42000000, v64
	v_mul_f32_e32 v163, 0x42000000, v52
	v_mul_f32_e32 v164, 0x42000000, v56
	v_cvt_pk_fp8_f32 v158, v162, v163
	v_mul_f32_e32 v165, 0x42000000, v44
	v_cvt_pk_fp8_f32 v158, v164, v165 op_sel:[0,0,1]
	v_mul_f32_e32 v162, 0x42000000, v48
	v_mul_f32_e32 v163, 0x42000000, v36
	v_mul_f32_e32 v164, 0x42000000, v40
	v_cvt_pk_fp8_f32 v159, v162, v163
	v_mul_f32_e32 v165, 0x42000000, v28
	v_cvt_pk_fp8_f32 v159, v164, v165 op_sel:[0,0,1]
	v_mul_f32_e32 v162, 0x42000000, v32
	v_mul_f32_e32 v163, 0x42000000, v20
	v_mul_f32_e32 v164, 0x42000000, v24
	v_cvt_pk_fp8_f32 v160, v162, v163
	v_mul_f32_e32 v165, 0x42000000, v12
	v_cvt_pk_fp8_f32 v160, v164, v165 op_sel:[0,0,1]
	v_mul_f32_e32 v162, 0x42000000, v16
	v_mul_f32_e32 v163, 0x42000000, v4
	v_mul_f32_e32 v164, 0x42000000, v8
	v_cvt_pk_fp8_f32 v161, v162, v163
	v_mul_f32_e32 v165, 0x42000000, v128
	v_cvt_pk_fp8_f32 v161, v164, v165 op_sel:[0,0,1]
	ds_write_b128 v156, v[158:161]
	v_mul_f32_e32 v162, 0x42000000, v65
	v_mul_f32_e32 v163, 0x42000000, v53
	v_mul_f32_e32 v164, 0x42000000, v57
	v_cvt_pk_fp8_f32 v168, v162, v163
	v_mul_f32_e32 v165, 0x42000000, v45
	v_cvt_pk_fp8_f32 v168, v164, v165 op_sel:[0,0,1]
	v_mul_f32_e32 v162, 0x42000000, v49
	v_mul_f32_e32 v163, 0x42000000, v37
	v_mul_f32_e32 v164, 0x42000000, v41
	v_cvt_pk_fp8_f32 v169, v162, v163
	v_mul_f32_e32 v165, 0x42000000, v29
	v_cvt_pk_fp8_f32 v169, v164, v165 op_sel:[0,0,1]
	v_mul_f32_e32 v162, 0x42000000, v33
	v_mul_f32_e32 v163, 0x42000000, v21
	v_mul_f32_e32 v164, 0x42000000, v25
	v_cvt_pk_fp8_f32 v170, v162, v163
	v_mul_f32_e32 v165, 0x42000000, v13
	v_cvt_pk_fp8_f32 v170, v164, v165 op_sel:[0,0,1]
	v_mul_f32_e32 v162, 0x42000000, v17
	v_mul_f32_e32 v163, 0x42000000, v5
	v_mul_f32_e32 v164, 0x42000000, v9
	v_cvt_pk_fp8_f32 v171, v162, v163
	v_mul_f32_e32 v165, 0x42000000, v129
	v_cvt_pk_fp8_f32 v171, v164, v165 op_sel:[0,0,1]
	ds_write_b128 v156, v[168:171] offset:256
	v_mul_f32_e32 v162, 0x42000000, v66
	v_mul_f32_e32 v163, 0x42000000, v54
	v_mul_f32_e32 v164, 0x42000000, v58
	v_cvt_pk_fp8_f32 v158, v162, v163
	v_mul_f32_e32 v165, 0x42000000, v46
	v_cvt_pk_fp8_f32 v158, v164, v165 op_sel:[0,0,1]
	v_mul_f32_e32 v162, 0x42000000, v50
	v_mul_f32_e32 v163, 0x42000000, v38
	v_mul_f32_e32 v164, 0x42000000, v42
	v_cvt_pk_fp8_f32 v159, v162, v163
	v_mul_f32_e32 v165, 0x42000000, v30
	v_cvt_pk_fp8_f32 v159, v164, v165 op_sel:[0,0,1]
	v_mul_f32_e32 v162, 0x42000000, v34
	v_mul_f32_e32 v163, 0x42000000, v22
	v_mul_f32_e32 v164, 0x42000000, v26
	v_cvt_pk_fp8_f32 v160, v162, v163
	v_mul_f32_e32 v165, 0x42000000, v14
	v_cvt_pk_fp8_f32 v160, v164, v165 op_sel:[0,0,1]
	v_mul_f32_e32 v162, 0x42000000, v18
	v_mul_f32_e32 v163, 0x42000000, v6
	v_mul_f32_e32 v164, 0x42000000, v10
	v_cvt_pk_fp8_f32 v161, v162, v163
	v_mul_f32_e32 v165, 0x42000000, v130
	v_cvt_pk_fp8_f32 v161, v164, v165 op_sel:[0,0,1]
	ds_write_b128 v156, v[158:161] offset:512
	v_mul_f32_e32 v162, 0x42000000, v67
	v_mul_f32_e32 v163, 0x42000000, v55
	v_mul_f32_e32 v164, 0x42000000, v59
	v_cvt_pk_fp8_f32 v168, v162, v163
	v_mul_f32_e32 v165, 0x42000000, v47
	v_cvt_pk_fp8_f32 v168, v164, v165 op_sel:[0,0,1]
	v_mul_f32_e32 v162, 0x42000000, v51
	v_mul_f32_e32 v163, 0x42000000, v39
	v_mul_f32_e32 v164, 0x42000000, v43
	v_cvt_pk_fp8_f32 v169, v162, v163
	v_mul_f32_e32 v165, 0x42000000, v31
	v_cvt_pk_fp8_f32 v169, v164, v165 op_sel:[0,0,1]
	v_mul_f32_e32 v162, 0x42000000, v35
	v_mul_f32_e32 v163, 0x42000000, v23
	v_mul_f32_e32 v164, 0x42000000, v27
	v_cvt_pk_fp8_f32 v170, v162, v163
	v_mul_f32_e32 v165, 0x42000000, v15
	v_cvt_pk_fp8_f32 v170, v164, v165 op_sel:[0,0,1]
	v_mul_f32_e32 v162, 0x42000000, v19
	v_mul_f32_e32 v163, 0x42000000, v7
	v_mul_f32_e32 v164, 0x42000000, v11
	v_cvt_pk_fp8_f32 v171, v162, v163
	v_mul_f32_e32 v165, 0x42000000, v131
	v_cvt_pk_fp8_f32 v171, v164, v165 op_sel:[0,0,1]
	ds_write_b128 v156, v[168:171] offset:768
	global_load_dwordx4 v[64:67], v[166:167], off nt
	v_lshl_add_u64 v[172:173], v[166:167], 0, s[42:43]
	global_load_dwordx4 v[52:55], v[172:173], off nt
	v_lshl_add_u64 v[166:167], v[172:173], 0, s[42:43]
	global_load_dwordx4 v[56:59], v[166:167], off nt
	v_lshl_add_u64 v[172:173], v[166:167], 0, s[42:43]
	global_load_dwordx4 v[44:47], v[172:173], off nt
	v_lshl_add_u64 v[166:167], v[172:173], 0, s[42:43]
	global_load_dwordx4 v[48:51], v[166:167], off nt
	v_lshl_add_u64 v[172:173], v[166:167], 0, s[42:43]
	global_load_dwordx4 v[36:39], v[172:173], off nt
	v_lshl_add_u64 v[166:167], v[172:173], 0, s[42:43]
	global_load_dwordx4 v[40:43], v[166:167], off nt
	v_lshl_add_u64 v[172:173], v[166:167], 0, s[42:43]
	global_load_dwordx4 v[28:31], v[172:173], off nt
	v_lshl_add_u64 v[166:167], v[172:173], 0, s[42:43]
	global_load_dwordx4 v[32:35], v[166:167], off nt
	v_lshl_add_u64 v[172:173], v[166:167], 0, s[42:43]
	global_load_dwordx4 v[20:23], v[172:173], off nt
	v_lshl_add_u64 v[166:167], v[172:173], 0, s[42:43]
	global_load_dwordx4 v[24:27], v[166:167], off nt
	v_lshl_add_u64 v[172:173], v[166:167], 0, s[42:43]
	global_load_dwordx4 v[12:15], v[172:173], off nt
	v_lshl_add_u64 v[166:167], v[172:173], 0, s[42:43]
	global_load_dwordx4 v[16:19], v[166:167], off nt
	v_lshl_add_u64 v[172:173], v[166:167], 0, s[42:43]
	global_load_dwordx4 v[4:7], v[172:173], off nt
	v_lshl_add_u64 v[166:167], v[172:173], 0, s[42:43]
	global_load_dwordx4 v[8:11], v[166:167], off nt
	v_lshl_add_u64 v[172:173], v[166:167], 0, s[42:43]
	global_load_dwordx4 v[128:131], v[172:173], off nt
	v_lshl_add_u64 v[166:167], v[172:173], 0, s[42:43]
	v_mov_b32_e32 v154, s61
	s_branch .Lcv_join
.Lcv_nonext:
	s_waitcnt vmcnt(8)
	v_mul_f32_e32 v162, 0x42000000, v64
	v_mul_f32_e32 v163, 0x42000000, v52
	v_mul_f32_e32 v164, 0x42000000, v56
	v_cvt_pk_fp8_f32 v158, v162, v163
	v_mul_f32_e32 v165, 0x42000000, v44
	v_cvt_pk_fp8_f32 v158, v164, v165 op_sel:[0,0,1]
	v_mul_f32_e32 v162, 0x42000000, v48
	v_mul_f32_e32 v163, 0x42000000, v36
	v_mul_f32_e32 v164, 0x42000000, v40
	v_cvt_pk_fp8_f32 v159, v162, v163
	v_mul_f32_e32 v165, 0x42000000, v28
	v_cvt_pk_fp8_f32 v159, v164, v165 op_sel:[0,0,1]
	v_mul_f32_e32 v162, 0x42000000, v32
	v_mul_f32_e32 v163, 0x42000000, v20
	v_mul_f32_e32 v164, 0x42000000, v24
	v_cvt_pk_fp8_f32 v160, v162, v163
	v_mul_f32_e32 v165, 0x42000000, v12
	v_cvt_pk_fp8_f32 v160, v164, v165 op_sel:[0,0,1]
	v_mul_f32_e32 v162, 0x42000000, v16
	v_mul_f32_e32 v163, 0x42000000, v4
	v_mul_f32_e32 v164, 0x42000000, v8
	v_cvt_pk_fp8_f32 v161, v162, v163
	v_mul_f32_e32 v165, 0x42000000, v128
	v_cvt_pk_fp8_f32 v161, v164, v165 op_sel:[0,0,1]
	ds_write_b128 v156, v[158:161]
	v_mul_f32_e32 v162, 0x42000000, v65
	v_mul_f32_e32 v163, 0x42000000, v53
	v_mul_f32_e32 v164, 0x42000000, v57
	v_cvt_pk_fp8_f32 v168, v162, v163
	v_mul_f32_e32 v165, 0x42000000, v45
	v_cvt_pk_fp8_f32 v168, v164, v165 op_sel:[0,0,1]
	v_mul_f32_e32 v162, 0x42000000, v49
	v_mul_f32_e32 v163, 0x42000000, v37
	v_mul_f32_e32 v164, 0x42000000, v41
	v_cvt_pk_fp8_f32 v169, v162, v163
	v_mul_f32_e32 v165, 0x42000000, v29
	v_cvt_pk_fp8_f32 v169, v164, v165 op_sel:[0,0,1]
	v_mul_f32_e32 v162, 0x42000000, v33
	v_mul_f32_e32 v163, 0x42000000, v21
	v_mul_f32_e32 v164, 0x42000000, v25
	v_cvt_pk_fp8_f32 v170, v162, v163
	v_mul_f32_e32 v165, 0x42000000, v13
	v_cvt_pk_fp8_f32 v170, v164, v165 op_sel:[0,0,1]
	v_mul_f32_e32 v162, 0x42000000, v17
	v_mul_f32_e32 v163, 0x42000000, v5
	v_mul_f32_e32 v164, 0x42000000, v9
	v_cvt_pk_fp8_f32 v171, v162, v163
	v_mul_f32_e32 v165, 0x42000000, v129
	v_cvt_pk_fp8_f32 v171, v164, v165 op_sel:[0,0,1]
	ds_write_b128 v156, v[168:171] offset:256
	v_mul_f32_e32 v162, 0x42000000, v66
	v_mul_f32_e32 v163, 0x42000000, v54
	v_mul_f32_e32 v164, 0x42000000, v58
	v_cvt_pk_fp8_f32 v158, v162, v163
	v_mul_f32_e32 v165, 0x42000000, v46
	v_cvt_pk_fp8_f32 v158, v164, v165 op_sel:[0,0,1]
	v_mul_f32_e32 v162, 0x42000000, v50
	v_mul_f32_e32 v163, 0x42000000, v38
	v_mul_f32_e32 v164, 0x42000000, v42
	v_cvt_pk_fp8_f32 v159, v162, v163
	v_mul_f32_e32 v165, 0x42000000, v30
	v_cvt_pk_fp8_f32 v159, v164, v165 op_sel:[0,0,1]
	v_mul_f32_e32 v162, 0x42000000, v34
	v_mul_f32_e32 v163, 0x42000000, v22
	v_mul_f32_e32 v164, 0x42000000, v26
	v_cvt_pk_fp8_f32 v160, v162, v163
	v_mul_f32_e32 v165, 0x42000000, v14
	v_cvt_pk_fp8_f32 v160, v164, v165 op_sel:[0,0,1]
	v_mul_f32_e32 v162, 0x42000000, v18
	v_mul_f32_e32 v163, 0x42000000, v6
	v_mul_f32_e32 v164, 0x42000000, v10
	v_cvt_pk_fp8_f32 v161, v162, v163
	v_mul_f32_e32 v165, 0x42000000, v130
	v_cvt_pk_fp8_f32 v161, v164, v165 op_sel:[0,0,1]
	ds_write_b128 v156, v[158:161] offset:512
	v_mul_f32_e32 v162, 0x42000000, v67
	v_mul_f32_e32 v163, 0x42000000, v55
	v_mul_f32_e32 v164, 0x42000000, v59
	v_cvt_pk_fp8_f32 v168, v162, v163
	v_mul_f32_e32 v165, 0x42000000, v47
	v_cvt_pk_fp8_f32 v168, v164, v165 op_sel:[0,0,1]
	v_mul_f32_e32 v162, 0x42000000, v51
	v_mul_f32_e32 v163, 0x42000000, v39
	v_mul_f32_e32 v164, 0x42000000, v43
	v_cvt_pk_fp8_f32 v169, v162, v163
	v_mul_f32_e32 v165, 0x42000000, v31
	v_cvt_pk_fp8_f32 v169, v164, v165 op_sel:[0,0,1]
	v_mul_f32_e32 v162, 0x42000000, v35
	v_mul_f32_e32 v163, 0x42000000, v23
	v_mul_f32_e32 v164, 0x42000000, v27
	v_cvt_pk_fp8_f32 v170, v162, v163
	v_mul_f32_e32 v165, 0x42000000, v15
	v_cvt_pk_fp8_f32 v170, v164, v165 op_sel:[0,0,1]
	v_mul_f32_e32 v162, 0x42000000, v19
	v_mul_f32_e32 v163, 0x42000000, v7
	v_mul_f32_e32 v164, 0x42000000, v11
	v_cvt_pk_fp8_f32 v171, v162, v163
	v_mul_f32_e32 v165, 0x42000000, v131
	v_cvt_pk_fp8_f32 v171, v164, v165 op_sel:[0,0,1]
	ds_write_b128 v156, v[168:171] offset:768
.Lcv_join:
	s_waitcnt lgkmcnt(0)
	s_barrier
	s_branch .LBB0_248
